# schedule: 790 conversion blocks per layer moved from the in_proj spare workgroups into the mixer phase
# speedup vs baseline: 1.0120x; 1.0120x over previous
.LBB0_310:
	s_lshl_b32 s4, s2, 3
	v_writelane_b32 v254, s4, 7
	s_lshl_b32 s4, s3, 3
	v_writelane_b32 v254, s4, 8
	s_lshl_b32 s4, s2, 9
	s_lshl_b32 s62, s3, 9
	s_cmp_eq_u32 s2, 0
	v_writelane_b32 v254, s4, 9
	s_cselect_b64 s[4:5], -1, 0
	v_writelane_b32 v254, s4, 10
	s_lshl_b32 s8, s2, 5
	s_and_b32 s14, s87, 31
	v_writelane_b32 v254, s5, 11
	s_mul_i32 s4, s2, 0x6b
	s_add_i32 s7, s4, 0xffffd954
	s_ashr_i32 s11, s87, 5
	s_lshl_b32 s4, s2, 4
	s_lshl_b32 s66, s3, 4
	s_cmpk_lt_i32 s2, 0x100
	v_writelane_b32 v254, s4, 12
	s_cselect_b64 s[4:5], -1, 0
	v_writelane_b32 v254, s4, 13
	s_movk_i32 s64, 0x80
	s_movk_i32 s65, 0xff00
	v_writelane_b32 v254, s5, 14
	s_lshr_b32 s4, s2, 3
	s_mul_i32 s4, s4, 5
	s_and_b32 s5, s2, 7
	s_add_i32 s4, s4, s5
	s_add_i32 s4, s4, -3
	s_cmp_lt_u32 s5, 3
	s_cselect_b32 s4, 0x7fff, s4
	s_cmpk_lt_i32 s4, 0x80
	v_writelane_b32 v254, s4, 15
	s_cselect_b64 s[4:5], -1, 0
	s_and_b32 s9, s87, 3
	v_writelane_b32 v254, s4, 16
	s_cmpk_lt_i32 s2, 0x200
	s_movk_i32 s56, 0x1000
	v_writelane_b32 v254, s5, 17
	s_cselect_b64 s[4:5], -1, 0
	v_writelane_b32 v254, s4, 18
	s_lshl_b32 s74, s3, 5
	s_movk_i32 s77, 0x4400
	v_writelane_b32 v254, s5, 19
	s_lshl_b32 s4, s2, 2
	s_and_b32 s4, s4, 0xffffff00
	v_writelane_b32 v254, s4, 20
	s_lshl_b32 s4, s2, 6
	s_and_b32 s6, s4, 0xfc0
	s_cmp_gt_i32 s3, 0
	v_writelane_b32 v254, s4, 21
	s_cselect_b64 s[4:5], -1, 0
	v_writelane_b32 v254, s4, 22
	s_ashr_i32 s12, s87, 2
	s_mov_b32 s10, s12
	v_writelane_b32 v254, s5, 23
	s_ashr_i32 s4, s87, 3
	v_writelane_b32 v254, s4, 24
	s_and_b32 s5, s87, 7
	s_lshl_b32 s4, s5, 7
	v_writelane_b32 v254, s5, 25
	s_lshl_b32 s5, s5, 18
	v_writelane_b32 v254, s5, 26
	s_ashr_i32 s13, s12, 31
	v_writelane_b32 v254, s10, 27
	s_lshl_b64 s[12:13], s[12:13], 18
	s_lshl_b32 s5, s9, 8
	v_writelane_b32 v254, s11, 28
	v_writelane_b32 v254, s12, 29
	s_mov_b32 s38, 0x78787879
	s_movk_i32 s39, 0xef00
	v_writelane_b32 v254, s13, 30
	v_writelane_b32 v254, s9, 31
	s_lshl_b32 s9, s9, 18
	s_cmpk_lt_i32 s2, 0x84
	v_writelane_b32 v254, s9, 32
	s_cselect_b32 s9, 32, 0x6b
	v_writelane_b32 v254, s9, 33
	v_writelane_b32 v254, s8, 34
	s_cselect_b32 s7, s8, s7
	v_writelane_b32 v254, s7, 35
	s_add_i32 s7, s3, -1
	s_cmp_gt_u32 s7, 6
	s_cselect_b64 s[8:9], -1, 0
	s_abs_i32 s12, s3
	v_cvt_f32_u32_e32 v1, s12
	v_writelane_b32 v254, s8, 36
	s_sub_i32 s7, 0, s12
	s_and_b32 s76, s3, 0x7ffffff8
	v_rcp_iflag_f32_e32 v1, v1
	v_writelane_b32 v254, s9, 37
	s_ashr_i32 s13, s3, 31
	s_mov_b32 s59, 0x800000
	v_mul_f32_e32 v1, 0x4f7ffffe, v1
	v_cvt_u32_f32_e32 v1, v1
	v_mov_b32_e32 v205, 1
	v_mov_b32_e32 v221, 0x1400
	v_mov_b32_e32 v204, 0x20200
	v_readfirstlane_b32 s8, v1
	s_mul_i32 s7, s7, s8
	s_mul_hi_u32 s7, s8, s7
	s_add_i32 s7, s8, s7
	v_writelane_b32 v254, s7, 38
	s_mul_hi_u32 s7, s7, 0x9e9
	s_mul_i32 s8, s7, s12
	s_sub_i32 s8, 0x9e9, s8
	s_add_i32 s9, s7, 1
	s_sub_i32 s10, s8, s12
	s_cmp_ge_u32 s8, s12
	s_cselect_b32 s7, s9, s7
	s_cselect_b32 s8, s10, s8
	s_add_i32 s9, s7, 1
	s_cmp_ge_u32 s8, s12
	s_cselect_b32 s7, s9, s7
	s_xor_b32 s7, s7, s13
	s_sub_i32 s7, s7, s13
	s_mul_i32 s8, s7, s3
	s_sub_i32 s8, 0x9e9, s8
	s_mul_i32 s9, s7, s87
	s_min_i32 s10, s87, s8
	v_writelane_b32 v254, s12, 39
	s_add_i32 s9, s9, s10
	v_writelane_b32 v254, s13, 40
	s_cmp_lt_i32 s87, s8
	v_writelane_b32 v254, s9, 41
	s_cselect_b64 s[8:9], -1, 0
	s_cmp_lg_u64 s[8:9], 0
	s_addc_u32 s7, s7, 0
	v_writelane_b32 v254, s7, 42
	s_lshl_b32 s7, s3, 1
	v_writelane_b32 v254, s7, 43
	s_add_i32 s7, s11, 17
	v_writelane_b32 v254, s7, 44
	s_lshl_b32 s7, s7, 4
	v_writelane_b32 v254, s7, 45
	s_lshl_b32 s7, s14, 4
	v_writelane_b32 v254, s14, 46
	s_add_i32 s8, s7, 0xd250
	v_writelane_b32 v254, s8, 47
	s_add_i32 s8, s11, 9
	v_writelane_b32 v254, s8, 48
	s_lshl_b32 s8, s8, 4
	v_writelane_b32 v254, s8, 49
	v_writelane_b32 v254, s11, 50
	s_add_i32 s8, s11, 1
	v_writelane_b32 v254, s8, 51
	s_or_b32 s8, s7, 0xfffffe00
	v_writelane_b32 v254, s8, 52
	s_lshl_b32 s8, s3, 6
	v_writelane_b32 v254, s8, 53
	s_add_i32 s7, s7, 0xa050
	v_writelane_b32 v254, s7, 54
	s_add_i32 s7, 0, 0x12000
	v_writelane_b32 v254, s7, 55
	s_add_i32 s7, 0, 0x27020
	v_writelane_b32 v254, s7, 56
	s_add_i32 s7, 0, 0x27024
	v_writelane_b32 v254, s7, 57
	s_add_i32 s7, 0, 0x25000
	v_writelane_b32 v254, s7, 58
	s_lshl_b32 s6, s6, 1
	v_writelane_b32 v254, s6, 59
	s_lshl_b32 s5, s5, 2
	v_writelane_b32 v254, s5, 60
	s_add_i32 s5, 0, 0x25400
	v_writelane_b32 v254, s5, 61
	s_add_i32 s5, 0, 0x10200
	v_writelane_b32 v254, s5, 62
	s_add_i32 s5, 0, 0x20100
	v_writelane_b32 v254, s5, 63
	s_add_i32 s5, 0, 0x20010
	v_writelane_b32 v255, s5, 0
	s_add_i32 s5, 0, 0x20110
	v_writelane_b32 v255, s5, 1
	s_add_i32 s5, 0, 0x20020
	v_writelane_b32 v255, s5, 2
	s_add_i32 s5, 0, 0x20120
	v_writelane_b32 v255, s5, 3
	s_add_i32 s5, 0, 0x20030
	v_writelane_b32 v255, s5, 4
	s_add_i32 s5, 0, 0x20130
	v_writelane_b32 v255, s5, 5
	s_add_i32 s5, 0, 0x20040
	v_writelane_b32 v255, s5, 6
	s_add_i32 s5, 0, 0x20140
	v_writelane_b32 v255, s5, 7
	s_add_i32 s5, 0, 0x20050
	v_writelane_b32 v255, s5, 8
	s_add_i32 s5, 0, 0x20150
	v_writelane_b32 v255, s5, 9
	s_add_i32 s5, 0, 0x20060
	v_writelane_b32 v255, s5, 10
	s_add_i32 s5, 0, 0x20160
	v_writelane_b32 v255, s5, 11
	s_add_i32 s5, 0, 0x20070
	v_writelane_b32 v255, s5, 12
	s_add_i32 s5, 0, 0x20170
	v_writelane_b32 v255, s5, 13
	s_add_i32 s5, 0, 0x20180
	v_writelane_b32 v255, s5, 14
	s_add_i32 s5, 0, 0x20084
	v_writelane_b32 v255, s5, 15
	s_add_i32 s5, 0, 0x20024
	v_writelane_b32 v255, s5, 16
	s_add_i32 s5, 0, 0x2002c
	v_writelane_b32 v255, s5, 17
	s_add_i32 s5, 0, 0x20034
	v_writelane_b32 v255, s5, 18
	s_add_i32 s5, 0, 0x2003c
	v_writelane_b32 v255, s5, 19
	s_add_i32 s5, 0, 0x20044
	v_writelane_b32 v255, s5, 20
	s_add_i32 s5, 0, 0x2004c
	v_writelane_b32 v255, s5, 21
	s_add_i32 s5, 0, 0x20054
	v_writelane_b32 v255, s5, 22
	s_add_i32 s5, 0, 0x2005c
	v_writelane_b32 v255, s5, 23
	s_add_i32 s5, 0, 0x20064
	v_writelane_b32 v255, s5, 24
	s_add_i32 s5, 0, 0x2006c
	v_writelane_b32 v255, s5, 25
	s_add_i32 s5, 0, 0x20074
	v_writelane_b32 v255, s5, 26
	s_add_i32 s5, 0, 0x2007c
	v_writelane_b32 v255, s5, 27
	s_add_i32 s5, 0, 0x20800
	v_writelane_b32 v255, s5, 28
	s_lshl_b32 s4, s4, 2
	v_writelane_b32 v255, s4, 29
	s_ashr_i32 s63, s62, 31
	s_ashr_i32 s67, s66, 31
	v_writelane_b32 v255, s5, 30
	v_cmp_eq_u32_e64 s[4:5], 0, v0
	s_mov_b32 s6, s74
	s_add_i32 s84, 0, 0x20004
	v_writelane_b32 v255, s4, 31
	s_add_i32 s69, 0, 0x2000c
	s_add_i32 s68, 0, 0x20014
	v_writelane_b32 v255, s5, 32
	s_lshl_b64 s[4:5], s[62:63], 2
	v_writelane_b32 v255, s4, 33
	s_add_i32 s49, 0, 0x2001c
	v_mov_b32_e32 v1, 0
	v_writelane_b32 v255, s5, 34
	s_lshl_b64 s[4:5], s[66:67], 12
	v_writelane_b32 v255, s4, 35
	v_mov_b32_e32 v220, 0xff800000
	s_movk_i32 s47, 0x3ff
	v_writelane_b32 v255, s5, 36
	v_writelane_b32 v255, s6, 37
	s_mov_b32 s83, 0x34400000
	s_mov_b32 s80, 0x36500000
	v_writelane_b32 v255, s7, 38
	s_mov_b32 s6, s62
	v_writelane_b32 v255, s6, 39
	s_movk_i32 s81, 0x7fff
	s_mov_b32 s57, 0x41000000
	v_writelane_b32 v255, s7, 40
	s_mov_b32 s6, s66
	v_writelane_b32 v255, s6, 41
	s_movk_i32 s33, 0xfefe
	s_mov_b32 s85, 0x900000
	v_writelane_b32 v255, s7, 42
	v_writelane_b32 v255, s76, 43
	v_writelane_b32 v255, s84, 44
	s_mov_b32 s72, 0xc0e00000
	s_mov_b32 s73, 0
	s_mov_b32 s71, 0
	s_mov_b64 s[4:5], -1
	s_mov_b64 s[78:79], 0x80
	s_mov_b32 s82, 0x3e38aa3b
	s_mov_b32 s88, 0xc01d265f
	s_mov_b32 s50, s69
	s_mov_b32 s86, s68
	s_mov_b32 s60, s49
	v_writelane_b32 v255, s87, 45
	s_branch .LBB0_314

.LBB0_561:
	s_and_b64 vcc, exec, s[16:17]
	s_cbranch_vccz .LBB0_711
	v_readlane_b32 s6, v254, 50
	v_readlane_b32 s7, v254, 46
	s_mul_i32 s6, s35, s6
	s_sub_i32 s7, s7, s36
	s_add_i32 s23, s7, s6
	s_lshl_b32 s22, s35, 3
	s_mov_b64 s[6:7], -1
	s_and_b64 vcc, exec, s[90:91]
	s_cbranch_vccz .LBB0_637
	v_mbcnt_lo_u32_b32 v66, -1, 0
	v_mbcnt_hi_u32_b32 v66, -1, v66
	s_getreg_b32 s6, hwreg(HW_REG_HW_ID, 0, 6)
	s_lshl_b32 s6, s6, 2
	s_and_b32 s6, s6, 0xfc
	s_or_b32 s6, s6, 0x27100
	v_mov_b32_e32 v0, s6
	ds_read_b32 v0, v0
	s_cmpk_gt_i32 s23, 0xd1
	s_waitcnt lgkmcnt(0)
	v_readfirstlane_b32 s9, v0
	s_cbranch_scc1 .LBB0_636
	s_add_i32 s20, s23, 0xd45
	s_mul_hi_i32 s6, s20, 0x2aaaaaab
	s_lshr_b32 s7, s6, 31
	s_ashr_i32 s15, s6, 9
	s_add_i32 s15, s15, s7
	s_mul_i32 s16, s15, 0xfffff400
	s_add_i32 s16, s16, s20
	s_cmpk_gt_i32 s16, 0x7ff
	s_mov_b64 s[12:13], -1
	s_cbranch_scc0 .LBB0_566
	s_add_i32 s6, s16, 0xfffff800
	s_mov_b32 s10, 31
	s_lshl_b32 s7, s15, 5
	s_lshr_b32 s6, s6, 5
	s_lshl_b32 s24, s20, 8
	s_ashr_i32 s11, s10, 31
	s_add_i32 s6, s6, s7
	s_lshl_b32 s14, s20, 5
	s_and_b32 s8, s24, 0x300
	s_lshl_b64 s[10:11], s[10:11], 3
	s_add_u32 s10, s0, s10
	s_addc_u32 s11, s1, s11
	s_load_dwordx2 s[10:11], s[10:11], 0x0
	s_ashr_i32 s7, s6, 31
	s_lshl_b64 s[12:13], s[6:7], 20
	s_lshl_b64 s[6:7], s[6:7], 22
	s_waitcnt lgkmcnt(0)
	s_add_u32 s6, s10, s6
	s_mov_b32 s10, 35
	s_addc_u32 s7, s11, s7
	s_ashr_i32 s11, s10, 31
	s_lshl_b64 s[10:11], s[10:11], 3
	s_add_u32 s10, s0, s10
	s_addc_u32 s11, s1, s11
	s_load_dwordx2 s[10:11], s[10:11], 0x0
	s_waitcnt lgkmcnt(0)
	s_add_u32 s10, s10, s12
	s_addc_u32 s11, s11, s13
	s_add_u32 s10, s10, 0x12800000
	s_addc_u32 s11, s11, 0
	s_mov_b64 s[12:13], 0

.LBB0_571:
	v_ashrrev_i32_e32 v139, 31, v138
	v_lshlrev_b64 v[138:139], 10, v[138:139]
	s_add_i32 s30, s30, s27
	v_readlane_b32 s6, v254, 46
	v_lshl_add_u64 v[138:139], s[16:17], 0, v[138:139]
	s_add_i32 s24, s24, s25
	s_add_i32 s26, s26, s27
	s_add_i32 s36, s36, s28
	s_add_i32 s29, s29, s27
	s_add_i32 s6, s6, s30
	v_lshl_add_u64 v[138:139], v[138:139], 0, s[14:15]
	s_cmpk_gt_i32 s6, 0xe16
	v_lshl_add_u64 v[138:139], v[138:139], 0, v[136:137]
	s_cselect_b64 s[6:7], -1, 0
	s_waitcnt lgkmcnt(0)
	global_store_dwordx4 v[138:139], v[130:133], off nt

.LBB0_573:
	v_readlane_b32 s6, v254, 46
	s_add_i32 s6, s6, s29
	s_add_i32 s9, s20, s22
	s_add_i32 s7, s6, 0xd25
	s_cmpk_lt_i32 s7, 0xe17
	s_cselect_b64 s[18:19], -1, 0
	s_cmpk_gt_i32 s7, 0xe16
	s_cbranch_scc1 .LBB0_580
	s_mul_hi_i32 s7, s7, 0x2aaaaaab
	s_lshr_b32 s12, s7, 31
	s_ashr_i32 s20, s7, 9
	s_add_i32 s20, s20, s12
	s_mul_i32 s7, s20, 0xfffff400
	s_add_i32 s37, s6, s7
	s_add_i32 s21, s37, 0xd25
	s_cmpk_gt_i32 s21, 0x7ff
	s_mov_b64 s[14:15], -1
	s_cbranch_scc0 .LBB0_576
	s_addk_i32 s37, 0x525
	s_mov_b32 s14, 31
	s_lshl_b32 s6, s20, 5
	s_lshr_b32 s7, s37, 5
	s_ashr_i32 s15, s14, 31
	s_add_i32 s6, s7, s6
	s_lshl_b32 s13, s9, 5
	s_and_b32 s12, s24, 0x300
	s_lshl_b64 s[14:15], s[14:15], 3
	s_add_u32 s14, s0, s14
	s_addc_u32 s15, s1, s15
	s_load_dwordx2 s[14:15], s[14:15], 0x0
	s_ashr_i32 s7, s6, 31
	s_lshl_b64 s[16:17], s[6:7], 20
	s_lshl_b64 s[6:7], s[6:7], 22
	s_waitcnt lgkmcnt(0)
	s_add_u32 s6, s14, s6
	s_mov_b32 s14, 35
	s_addc_u32 s7, s15, s7
	s_ashr_i32 s15, s14, 31
	s_lshl_b64 s[14:15], s[14:15], 3
	s_add_u32 s14, s0, s14
	s_addc_u32 s15, s1, s15
	s_load_dwordx2 s[14:15], s[14:15], 0x0
	s_waitcnt lgkmcnt(0)
	s_add_u32 s14, s14, s16
	s_addc_u32 s15, s15, s17
	s_add_u32 s16, s14, 0x12800000
	s_addc_u32 s17, s15, 0
	s_mov_b64 s[14:15], 0

.LBB0_604:
	v_ashrrev_i32_e32 v139, 31, v138
	v_lshlrev_b64 v[138:139], 10, v[138:139]
	v_lshl_add_u64 v[138:139], s[10:11], 0, v[138:139]
	v_lshl_add_u64 v[138:139], v[138:139], 0, s[70:71]
	v_lshl_add_u64 v[138:139], v[138:139], 0, v[136:137]
	s_andn2_b64 vcc, exec, s[18:19]
	s_mov_b64 s[6:7], -1
	s_waitcnt lgkmcnt(0)
	global_store_dwordx4 v[138:139], v[130:133], off nt
	s_cbranch_vccnz .LBB0_572
	v_readlane_b32 s6, v254, 46
	s_add_i32 s6, s6, s26
	s_add_i32 s20, s9, s22
	s_add_i32 s7, s6, 0xd25
	s_cmpk_gt_i32 s7, 0xe16
	s_cbranch_scc1 .LBB0_612
	s_mul_hi_i32 s7, s7, 0x2aaaaaab
	s_lshr_b32 s8, s7, 31
	s_ashr_i32 s13, s7, 9
	s_add_i32 s13, s13, s8
	s_mul_i32 s7, s13, 0xfffff400
	s_add_i32 s21, s6, s7
	s_add_i32 s15, s21, 0xd25
	s_cmpk_gt_i32 s15, 0x7ff
	s_mov_b64 s[18:19], -1
	s_cbranch_scc0 .LBB0_608
	s_addk_i32 s21, 0x525
	s_mov_b32 s10, 31
	s_lshl_b32 s6, s13, 5
	s_lshr_b32 s7, s21, 5
	s_ashr_i32 s11, s10, 31
	s_add_i32 s6, s7, s6
	s_lshl_b32 s9, s20, 5
	s_and_b32 s8, s24, 0x300
	s_lshl_b64 s[10:11], s[10:11], 3
	s_add_u32 s10, s0, s10
	s_addc_u32 s11, s1, s11
	s_load_dwordx2 s[10:11], s[10:11], 0x0
	s_ashr_i32 s7, s6, 31
	s_lshl_b64 s[18:19], s[6:7], 20
	s_lshl_b64 s[6:7], s[6:7], 22
	s_waitcnt lgkmcnt(0)
	s_add_u32 s6, s10, s6
	s_mov_b32 s10, 35
	s_addc_u32 s7, s11, s7
	s_ashr_i32 s11, s10, 31
	s_lshl_b64 s[10:11], s[10:11], 3
	s_add_u32 s10, s0, s10
	s_addc_u32 s11, s1, s11
	s_load_dwordx2 s[10:11], s[10:11], 0x0
	s_waitcnt lgkmcnt(0)
	s_add_u32 s10, s10, s18
	s_addc_u32 s11, s11, s19
	s_add_u32 s10, s10, 0x12800000
	s_addc_u32 s11, s11, 0
	s_mov_b64 s[18:19], 0

.LBB0_637:
	s_andn2_b64 vcc, exec, s[6:7]
	s_cbranch_vccnz .LBB0_711
	v_mbcnt_lo_u32_b32 v66, -1, 0
	v_mbcnt_hi_u32_b32 v66, -1, v66
	s_getreg_b32 s6, hwreg(HW_REG_HW_ID, 0, 6)
	s_lshl_b32 s6, s6, 2
	s_and_b32 s6, s6, 0xfc
	s_or_b32 s6, s6, 0x27100
	v_mov_b32_e32 v0, s6
	ds_read_b32 v0, v0
	s_cmpk_gt_i32 s23, 0x3b
	s_waitcnt lgkmcnt(0)
	v_readfirstlane_b32 s9, v0
	s_cbranch_scc1 .LBB0_711
	s_mul_hi_i32 s6, s23, 0x2aaaaaab
	s_lshr_b32 s7, s6, 31
	s_ashr_i32 s15, s6, 9
	s_add_i32 s15, s15, s7
	s_mul_i32 s16, s15, 0xfffff400
	s_add_i32 s16, s16, s23
	s_cmpk_gt_i32 s16, 0x7ff
	s_mov_b64 s[12:13], -1
	s_cbranch_scc0 .LBB0_641
	s_add_i32 s6, s16, 0xfffff800
	s_mov_b32 s10, 31
	s_lshl_b32 s7, s15, 5
	s_lshr_b32 s6, s6, 5
	s_lshl_b32 s24, s23, 8
	s_ashr_i32 s11, s10, 31
	s_add_i32 s6, s6, s7
	s_lshl_b32 s14, s23, 5
	s_and_b32 s8, s24, 0x300
	s_lshl_b64 s[10:11], s[10:11], 3
	s_add_u32 s10, s0, s10
	s_addc_u32 s11, s1, s11
	s_load_dwordx2 s[10:11], s[10:11], 0x0
	s_ashr_i32 s7, s6, 31
	s_lshl_b64 s[12:13], s[6:7], 20
	s_lshl_b64 s[6:7], s[6:7], 22
	s_waitcnt lgkmcnt(0)
	s_add_u32 s6, s10, s6
	s_mov_b32 s10, 35
	s_addc_u32 s7, s11, s7
	s_ashr_i32 s11, s10, 31
	s_lshl_b64 s[10:11], s[10:11], 3
	s_add_u32 s10, s0, s10
	s_addc_u32 s11, s1, s11
	s_load_dwordx2 s[10:11], s[10:11], 0x0
	s_waitcnt lgkmcnt(0)
	s_add_u32 s10, s10, s12
	s_addc_u32 s11, s11, s13
	s_add_u32 s10, s10, 0x12800000
	s_addc_u32 s11, s11, 0
	s_mov_b64 s[12:13], 0

.LBB0_646:
	v_ashrrev_i32_e32 v139, 31, v138
	v_lshlrev_b64 v[138:139], 10, v[138:139]
	s_add_i32 s35, s35, s27
	v_readlane_b32 s6, v254, 46
	v_lshl_add_u64 v[138:139], s[16:17], 0, v[138:139]
	s_add_i32 s24, s24, s25
	s_add_i32 s26, s26, s27
	s_add_i32 s37, s37, s29
	s_add_i32 s30, s30, s27
	s_add_i32 s6, s6, s35
	v_lshl_add_u64 v[138:139], v[138:139], 0, s[14:15]
	s_cmpk_gt_i32 s6, 0x3b
	v_lshl_add_u64 v[138:139], v[138:139], 0, v[136:137]
	s_cselect_b64 s[6:7], -1, 0
	s_waitcnt lgkmcnt(0)
	global_store_dwordx4 v[138:139], v[130:133], off nt

.LBB0_648:
	v_readlane_b32 s6, v254, 46
	s_add_i32 s6, s6, s30
	s_add_i32 s9, s23, s22
	s_sub_i32 s7, s6, 32
	s_cmpk_lt_i32 s7, 0x3c
	s_cselect_b64 s[18:19], -1, 0
	s_cmpk_gt_i32 s7, 0x3b
	s_cbranch_scc1 .LBB0_655
	s_mul_hi_i32 s7, s7, 0x2aaaaaab
	s_lshr_b32 s12, s7, 31
	s_ashr_i32 s20, s7, 9
	s_add_i32 s20, s20, s12
	s_mul_i32 s7, s20, 0xfffff400
	s_add_i32 s23, s6, s7
	s_sub_i32 s21, s23, 32
	s_cmpk_gt_i32 s21, 0x7ff
	s_mov_b64 s[14:15], -1
	s_cbranch_scc0 .LBB0_651
	s_addk_i32 s23, 0xf7e0
	s_mov_b32 s14, 31
	s_lshl_b32 s6, s20, 5
	s_lshr_b32 s7, s23, 5
	s_ashr_i32 s15, s14, 31
	s_add_i32 s6, s7, s6
	s_lshl_b32 s13, s9, 5
	s_and_b32 s12, s24, 0x300
	s_lshl_b64 s[14:15], s[14:15], 3
	s_add_u32 s14, s0, s14
	s_addc_u32 s15, s1, s15
	s_load_dwordx2 s[14:15], s[14:15], 0x0
	s_ashr_i32 s7, s6, 31
	s_lshl_b64 s[16:17], s[6:7], 20
	s_lshl_b64 s[6:7], s[6:7], 22
	s_waitcnt lgkmcnt(0)
	s_add_u32 s6, s14, s6
	s_mov_b32 s14, 35
	s_addc_u32 s7, s15, s7
	s_ashr_i32 s15, s14, 31
	s_lshl_b64 s[14:15], s[14:15], 3
	s_add_u32 s14, s0, s14
	s_addc_u32 s15, s1, s15
	s_load_dwordx2 s[14:15], s[14:15], 0x0
	s_waitcnt lgkmcnt(0)
	s_add_u32 s14, s14, s16
	s_addc_u32 s15, s15, s17
	s_add_u32 s16, s14, 0x12800000
	s_addc_u32 s17, s15, 0
	s_mov_b64 s[14:15], 0

.LBB0_679:
	v_ashrrev_i32_e32 v139, 31, v138
	v_lshlrev_b64 v[138:139], 10, v[138:139]
	v_lshl_add_u64 v[138:139], s[10:11], 0, v[138:139]
	v_lshl_add_u64 v[138:139], v[138:139], 0, s[70:71]
	v_lshl_add_u64 v[138:139], v[138:139], 0, v[136:137]
	s_andn2_b64 vcc, exec, s[18:19]
	s_mov_b64 s[6:7], -1
	s_waitcnt lgkmcnt(0)
	global_store_dwordx4 v[138:139], v[130:133], off nt
	s_cbranch_vccnz .LBB0_647
	v_readlane_b32 s6, v254, 46
	s_add_i32 s6, s6, s26
	s_add_i32 s23, s9, s22
	s_sub_i32 s7, s6, 32
	s_cmpk_gt_i32 s7, 0x3b
	s_cbranch_scc1 .LBB0_687
	s_mul_hi_i32 s7, s7, 0x2aaaaaab
	s_lshr_b32 s8, s7, 31
	s_ashr_i32 s13, s7, 9
	s_add_i32 s13, s13, s8
	s_mul_i32 s7, s13, 0xfffff400
	s_add_i32 s20, s6, s7
	s_sub_i32 s15, s20, 32
	s_cmpk_gt_i32 s15, 0x7ff
	s_mov_b64 s[18:19], -1
	s_cbranch_scc0 .LBB0_683
	s_addk_i32 s20, 0xf7e0
	s_mov_b32 s10, 31
	s_lshl_b32 s6, s13, 5
	s_lshr_b32 s7, s20, 5
	s_ashr_i32 s11, s10, 31
	s_add_i32 s6, s7, s6
	s_lshl_b32 s9, s23, 5
	s_and_b32 s8, s24, 0x300
	s_lshl_b64 s[10:11], s[10:11], 3
	s_add_u32 s10, s0, s10
	s_addc_u32 s11, s1, s11
	s_load_dwordx2 s[10:11], s[10:11], 0x0
	s_ashr_i32 s7, s6, 31
	s_lshl_b64 s[18:19], s[6:7], 20
	s_lshl_b64 s[6:7], s[6:7], 22
	s_waitcnt lgkmcnt(0)
	s_add_u32 s6, s10, s6
	s_mov_b32 s10, 35
	s_addc_u32 s7, s11, s7
	s_ashr_i32 s11, s10, 31
	s_lshl_b64 s[10:11], s[10:11], 3
	s_add_u32 s10, s0, s10
	s_addc_u32 s11, s1, s11
	s_load_dwordx2 s[10:11], s[10:11], 0x0
	s_waitcnt lgkmcnt(0)
	s_add_u32 s10, s10, s18
	s_addc_u32 s11, s11, s19
	s_add_u32 s10, s10, 0x12800000
	s_addc_u32 s11, s11, 0
	s_mov_b64 s[18:19], 0

.LBB0_922:
	s_andn2_b64 vcc, exec, s[54:55]
	s_mov_b32 s43, 0
	s_cbranch_vccnz .LBB0_924
	s_and_b64 s[6:7], s[4:5], exec
	s_movk_i32 s6, 0x3c
	s_cselect_b32 s6, s6, 0xe17
	v_readlane_b32 s7, v254, 41
	s_add_i32 s43, s6, s7
